# down-unit hand-off wait: the two completion-counter polls issued together (one round trip)
# baseline (speedup 1.0000x reference)
; __device__ __forceinline__ void phase_moe_down(const Ptrs& p, LAS unsigned char* lds) {
;     ...
;                 for (unsigned sp = 0; sp < (1u << 22); ++sp) {
;                     if (__hip_atomic_load(tot, __ATOMIC_RELAXED, __HIP_MEMORY_SCOPE_AGENT) >= (unsigned)Ugu) { all = 1; break; }
;                     if (__hip_atomic_load(de, __ATOMIC_RELAXED, __HIP_MEMORY_SCOPE_AGENT) >= need) break;
;                     __builtin_amdgcn_s_sleep(8); }
.LBB0_1455:
	global_load_dword v3, v2, s[30:31] offset:1024 sc1
	global_load_dword v236, v2, s[4:5] offset:2048 sc1
	s_waitcnt vmcnt(0)
	v_cmp_le_u32_e32 vcc, s21, v3
	s_cbranch_vccnz .LBB0_1473
	v_cmp_gt_u32_e32 vcc, s2, v236
	s_cbranch_vccz .LBB0_1474
	s_sleep 8
	global_load_dword v3, v2, s[30:31] offset:1024 sc1
	s_waitcnt vmcnt(0)
	v_cmp_gt_u32_e32 vcc, s21, v3
	s_cbranch_vccz .LBB0_1473
	global_load_dword v3, v2, s[4:5] offset:2048 sc1
	s_waitcnt vmcnt(0)
	v_cmp_gt_u32_e32 vcc, s2, v3
	s_cbranch_vccz .LBB0_1474
	s_sleep 8
	global_load_dword v3, v2, s[30:31] offset:1024 sc1
	s_waitcnt vmcnt(0)
	v_cmp_gt_u32_e32 vcc, s21, v3
	s_cbranch_vccz .LBB0_1473
	global_load_dword v3, v2, s[4:5] offset:2048 sc1
	s_waitcnt vmcnt(0)
	v_cmp_gt_u32_e32 vcc, s2, v3
	s_cbranch_vccz .LBB0_1474
	s_sleep 8
	global_load_dword v3, v2, s[30:31] offset:1024 sc1
	s_waitcnt vmcnt(0)
	v_cmp_gt_u32_e32 vcc, s21, v3
	s_cbranch_vccz .LBB0_1473
	global_load_dword v3, v2, s[4:5] offset:2048 sc1
	s_waitcnt vmcnt(0)
	v_cmp_gt_u32_e32 vcc, s2, v3
	s_cbranch_vccz .LBB0_1474
	s_sleep 8
	global_load_dword v3, v2, s[30:31] offset:1024 sc1
	s_waitcnt vmcnt(0)
	v_cmp_gt_u32_e32 vcc, s21, v3
	s_cbranch_vccz .LBB0_1473
	global_load_dword v3, v2, s[4:5] offset:2048 sc1
	s_waitcnt vmcnt(0)
	v_cmp_gt_u32_e32 vcc, s2, v3
	s_cbranch_vccz .LBB0_1474
	s_sleep 8
	global_load_dword v3, v2, s[30:31] offset:1024 sc1
	s_waitcnt vmcnt(0)
	v_cmp_gt_u32_e32 vcc, s21, v3
	s_cbranch_vccz .LBB0_1473
	global_load_dword v3, v2, s[4:5] offset:2048 sc1
	s_waitcnt vmcnt(0)
	v_cmp_gt_u32_e32 vcc, s2, v3
	s_cbranch_vccz .LBB0_1474
	s_sleep 8
	global_load_dword v3, v2, s[30:31] offset:1024 sc1
	s_waitcnt vmcnt(0)
	v_cmp_gt_u32_e32 vcc, s21, v3
	s_cbranch_vccz .LBB0_1473
	global_load_dword v3, v2, s[4:5] offset:2048 sc1
	s_waitcnt vmcnt(0)
	v_cmp_gt_u32_e32 vcc, s2, v3
	s_cbranch_vccz .LBB0_1474
	s_sleep 8
	global_load_dword v3, v2, s[30:31] offset:1024 sc1
	s_waitcnt vmcnt(0)
	v_cmp_gt_u32_e32 vcc, s21, v3
	s_cbranch_vccz .LBB0_1473
	global_load_dword v3, v2, s[4:5] offset:2048 sc1
	s_mov_b64 s[6:7], -1
	s_waitcnt vmcnt(0)
	v_cmp_gt_u32_e32 vcc, s2, v3
	s_cbranch_vccz .LBB0_1472
	s_add_i32 s3, s3, -8
	s_cmp_eq_u32 s3, 0
	s_cselect_b64 s[6:7], -1, 0
	s_sleep 8
